# attention tile software-pipelined across the two 64-key sub-tiles: QK of the next sub-tile and PV of the previous one interleaved with exp/cvt; K fragments staged in spare VGPRs; first LDS reads issue
# speedup vs baseline: 1.0096x; 1.0096x over previous
; #define LAS __attribute__((address_space(3)))
; __device__ __forceinline__ void map_tile(const LAS unsigned char* kp, int ko0, int ko1, const bf16x8 (&qf)[2], const s16x4 (&vlo)[8], const s16x4 (&vhi)[8], f32x16 (&o)[2], float& l) {
;     const bf16x8 k00 = *(const LAS bf16x8*)(kp + ko0), k01 = *(const LAS bf16x8*)(kp + ko1), k10 = *(const LAS bf16x8*)(kp + ko0 + 4096), k11 = *(const LAS bf16x8*)(kp + ko1 + 4096);
;     f32x16 z;
; #pragma unroll
;     for (int i = 0; i < 16; ++i) z[i] = 0.f;
;     f32x16 s0 = FA_MFMA(k00, qf[0], z), s1 = FA_MFMA(k10, qf[0], z);
;     __builtin_amdgcn_sched_group_barrier(0x8, 2, 0);
;     s0 = FA_MFMA(k01, qf[1], s0); s1 = FA_MFMA(k11, qf[1], s1);
; #pragma unroll
;     for (int i = 0; i < 16; ++i) { s0[i] = __builtin_amdgcn_exp2f(s0[i]); s1[i] = __builtin_amdgcn_exp2f(s1[i]); }
;     float a = 0.f, b = 0.f;
; #pragma unroll
;     for (int i = 0; i < 16; ++i) { a += s0[i]; b += s1[i]; }
;     l += a + b;
;     u32x4 pw[4];
; #pragma unroll
;     for (int j = 0; j < 4; ++j) { pw[0][j] = cvtpk(s0[2 * j], s0[2 * j + 1]); pw[1][j] = cvtpk(s0[8 + 2 * j], s0[8 + 2 * j + 1]); pw[2][j] = cvtpk(s1[2 * j], s1[2 * j + 1]); pw[3][j] = cvtpk(s1[8 + 2 * j], s1[8 + 2 * j + 1]); }
; #pragma unroll
;     for (int ks = 0; ks < 4; ++ks)
; #pragma unroll
;         for (int d0 = 0; d0 < 2; ++d0) {
;             const int i = d0 * 4 + ks;
; template <class Mid> __device__ __forceinline__ void attn_unit(const Mid& mid, LAS unsigned char* lds, const bf16* __restrict__ Qu, const bf16* __restrict__ Kh, const bf16* __restrict__ Vh, int q0, int NT, ...
;     ...
;     for (int t = 0; t < NT2; ++t) {
;         FA_WAIT_BAR(4);
;         { const int tn = (t + PFD < NT2) ? t + PFD : NT2 - 1; const int sn = (sl == 0) ? (NSLOT - 1) * SLOTB : sl - SLOTB; FA_DMA(tn, sn); }
; #pragma unroll 1
;         for (int sb = 0; sb < 2; ++sb) {
;             const LAS unsigned char* kp = kp0 + sl + sb * SUBB; const LAS unsigned char* vp = vp0 + sl + sb * SUBB;
;             s16x4 vlo[8], vhi[8];
; #pragma unroll
;             for (int i = 0; i < 8; ++i) { vlo[i] = vtr(vp + (i >> 2) * 4096 + (i & 3) * 1024); vhi[i] = vtr(vp + (i >> 2) * 4096 + (i & 3) * 1024 + 512); }
;             map_tile(kp, ko10, ko11, q1f, vlo, vhi, o1, l1);
;             map_tile(kp, ko20, ko21, q2f, vlo, vhi, o2, l2);
;             __builtin_amdgcn_sched_barrier(0);
;         }
.LBB0_460:
	s_add_i32 s14, s73, 2
	s_min_u32 s14, s14, s71
	s_add_i32 s28, s72, 0xffff8000
	s_cmp_lg_u32 s72, 0
	s_waitcnt vmcnt(4) lgkmcnt(0)
	s_barrier
	v_add_u32_e32 v196, s72, v214
	v_add_u32_e32 v220, s72, v219
	v_add_u32_e32 v126, v196, v215
	v_add_u32_e32 v127, v196, v217
	v_add_u32_e32 v192, v196, v216
	v_add_u32_e32 v193, v196, v218
	ds_read_b128 v[164:167], v126
	ds_read_b128 v[168:171], v127
	ds_read_b128 v[172:175], v126 offset:4096
	ds_read_b128 v[230:233], v127 offset:4096
	ds_read_b64_tr_b16 v[114:115], v220 offset:8192
	ds_read_b64_tr_b16 v[116:117], v220 offset:8704
	ds_read_b64_tr_b16 v[184:185], v220 offset:12288
	ds_read_b64_tr_b16 v[186:187], v220 offset:12800
	s_cselect_b32 s28, s28, 0x10000
	s_lshl_b32 s14, s14, 14
	s_add_i32 s29, s28, s49
	v_lshl_add_u64 v[66:67], v[176:177], 0, s[14:15]
	s_mov_b32 s74, m0
	s_mov_b32 m0, s29
	s_nop 0
	global_load_lds_dwordx4 v[66:67], off
	s_mov_b32 m0, s74
	s_add_i32 s28, s28, s70
	v_lshl_add_u64 v[66:67], v[178:179], 0, s[14:15]
	s_mov_b32 s74, m0
	s_mov_b32 m0, s28
	s_nop 0
	global_load_lds_dwordx4 v[66:67], off
	s_mov_b32 m0, s74
	s_bitset1_b32 s14, 13
	v_lshl_add_u64 v[66:67], v[176:177], 0, s[14:15]
	s_addk_i32 s29, 0x4000
	s_mov_b32 s74, m0
	s_mov_b32 m0, s29
	s_nop 0
	global_load_lds_dwordx4 v[66:67], off
	s_mov_b32 m0, s74
	v_lshl_add_u64 v[66:67], v[178:179], 0, s[14:15]
	s_add_i32 s14, s28, 0x4000
	s_mov_b32 s28, m0
	s_mov_b32 m0, s14
	s_nop 0
	global_load_lds_dwordx4 v[66:67], off
	s_mov_b32 m0, s28
	s_waitcnt lgkmcnt(7)
	v_mfma_f32_32x32x16_bf16 v[66:81], v[164:167], v[140:143], 0
	ds_read_b128 v[164:167], v192
	s_waitcnt lgkmcnt(7)
	v_mfma_f32_32x32x16_bf16 v[66:81], v[168:171], v[136:139], v[66:81]
	ds_read_b128 v[168:171], v193
	ds_read_b64_tr_b16 v[118:119], v220 offset:9216
	ds_read_b64_tr_b16 v[120:121], v220 offset:9728
	ds_read_b64_tr_b16 v[188:189], v220 offset:13312
	ds_read_b64_tr_b16 v[190:191], v220 offset:13824
	s_waitcnt lgkmcnt(11)
	v_mfma_f32_32x32x16_bf16 v[82:97], v[172:175], v[140:143], 0
	ds_read_b128 v[172:175], v192 offset:4096
	s_waitcnt lgkmcnt(11)
	v_mfma_f32_32x32x16_bf16 v[82:97], v[230:233], v[136:139], v[82:97]
	ds_read_b128 v[230:233], v193 offset:4096
	ds_read_b64_tr_b16 v[122:123], v220 offset:10240
	ds_read_b64_tr_b16 v[124:125], v220 offset:10752
	ds_read_b64_tr_b16 v[222:223], v220 offset:14336
	s_waitcnt lgkmcnt(14)
	ds_read_b64_tr_b16 v[224:225], v220 offset:14848
	s_nop 1
	s_waitcnt lgkmcnt(14)
	ds_read_b64_tr_b16 v[180:181], v220 offset:11264
	s_waitcnt lgkmcnt(14)
	ds_read_b64_tr_b16 v[182:183], v220 offset:11776
	s_waitcnt lgkmcnt(14)
	ds_read_b64_tr_b16 v[226:227], v220 offset:15360
	s_waitcnt lgkmcnt(14)
	ds_read_b64_tr_b16 v[228:229], v220 offset:15872
	v_exp_f32_e32 v66, v66
	v_exp_f32_e32 v67, v67
	v_exp_f32_e32 v68, v68
	v_exp_f32_e32 v69, v69
	v_cvt_pk_bf16_f32 v66, v66, v67
	v_cvt_pk_bf16_f32 v67, v68, v69
	v_exp_f32_e32 v70, v70
	v_exp_f32_e32 v71, v71
	v_exp_f32_e32 v72, v72
	v_mfma_f32_32x32x16_bf16 v[98:113], v[164:167], v[132:135], 0
	s_waitcnt lgkmcnt(14)
	ds_read_b128 v[164:167], v126 offset:16384
	v_exp_f32_e32 v73, v73
	v_cvt_pk_bf16_f32 v68, v70, v71
	v_cvt_pk_bf16_f32 v69, v72, v73
	v_exp_f32_e32 v74, v74
	v_exp_f32_e32 v75, v75
	v_mfma_f32_32x32x16_bf16 v[50:65], v[66:69], v[114:117], v[50:65]
	v_exp_f32_e32 v76, v76
	v_exp_f32_e32 v77, v77
	v_cvt_pk_bf16_f32 v70, v74, v75
	v_mfma_f32_32x32x16_bf16 v[34:49], v[66:69], v[184:187], v[34:49]
	v_cvt_pk_bf16_f32 v71, v76, v77
	v_exp_f32_e32 v78, v78
	v_exp_f32_e32 v79, v79
	v_mfma_f32_16x16x32_bf16 v[160:163], v[66:69], v[238:241], v[160:163]
	v_exp_f32_e32 v80, v80
	v_mfma_f32_32x32x16_bf16 v[98:113], v[168:171], v[128:131], v[98:113]
	s_waitcnt lgkmcnt(14)
	ds_read_b128 v[168:171], v127 offset:16384
	v_exp_f32_e32 v81, v81
	v_cvt_pk_bf16_f32 v72, v78, v79
	v_cvt_pk_bf16_f32 v73, v80, v81
	v_exp_f32_e32 v82, v82
	v_exp_f32_e32 v83, v83
	s_waitcnt lgkmcnt(14)
	v_mfma_f32_32x32x16_bf16 v[50:65], v[70:73], v[118:121], v[50:65]
	v_exp_f32_e32 v84, v84
	v_exp_f32_e32 v85, v85
	v_cvt_pk_bf16_f32 v82, v82, v83
	s_waitcnt lgkmcnt(12)
	v_mfma_f32_32x32x16_bf16 v[34:49], v[70:73], v[188:191], v[34:49]
	v_cvt_pk_bf16_f32 v83, v84, v85
	v_exp_f32_e32 v86, v86
	v_exp_f32_e32 v87, v87
	v_mfma_f32_16x16x32_bf16 v[160:163], v[70:73], v[238:241], v[160:163]
	v_exp_f32_e32 v88, v88
	s_waitcnt lgkmcnt(11)
	v_mfma_f32_32x32x16_bf16 v[144:159], v[172:175], v[132:135], 0
	ds_read_b128 v[172:175], v126 offset:20480
	v_exp_f32_e32 v89, v89
	v_cvt_pk_bf16_f32 v84, v86, v87
	v_cvt_pk_bf16_f32 v85, v88, v89
	v_exp_f32_e32 v90, v90
	v_exp_f32_e32 v91, v91
	s_waitcnt lgkmcnt(9)
	v_mfma_f32_32x32x16_bf16 v[50:65], v[82:85], v[122:125], v[50:65]
	v_exp_f32_e32 v92, v92
	v_exp_f32_e32 v93, v93
	v_cvt_pk_bf16_f32 v86, v90, v91
	s_waitcnt lgkmcnt(7)
	v_mfma_f32_32x32x16_bf16 v[34:49], v[82:85], v[222:225], v[34:49]
	v_cvt_pk_bf16_f32 v87, v92, v93
	v_exp_f32_e32 v94, v94
	v_exp_f32_e32 v95, v95
	v_mfma_f32_16x16x32_bf16 v[160:163], v[82:85], v[238:241], v[160:163]
	v_exp_f32_e32 v96, v96
	v_mfma_f32_32x32x16_bf16 v[144:159], v[230:233], v[128:131], v[144:159]
	ds_read_b128 v[230:233], v127 offset:20480
	v_exp_f32_e32 v97, v97
	v_cvt_pk_bf16_f32 v88, v94, v95
	v_cvt_pk_bf16_f32 v89, v96, v97
	v_exp_f32_e32 v98, v98
	v_exp_f32_e32 v99, v99
	s_waitcnt lgkmcnt(6)
	v_mfma_f32_32x32x16_bf16 v[50:65], v[86:89], v[180:183], v[50:65]
	v_exp_f32_e32 v100, v100
	v_exp_f32_e32 v101, v101
	v_cvt_pk_bf16_f32 v98, v98, v99
	s_waitcnt lgkmcnt(4)
	v_mfma_f32_32x32x16_bf16 v[34:49], v[86:89], v[226:229], v[34:49]
	v_cvt_pk_bf16_f32 v99, v100, v101
	v_exp_f32_e32 v102, v102
	v_exp_f32_e32 v103, v103
	v_mfma_f32_16x16x32_bf16 v[160:163], v[86:89], v[238:241], v[160:163]
	v_exp_f32_e32 v104, v104
	s_waitcnt lgkmcnt(3)
; #define LAS __attribute__((address_space(3)))
; #define FA_MFMA(a, b, c) __builtin_amdgcn_mfma_f32_32x32x16_bf16((a), (b), (c), 0, 0, 0)
; __device__ __forceinline__ void map_tile(const LAS unsigned char* kp, int ko0, int ko1, const bf16x8 (&qf)[2], const s16x4 (&vlo)[8], const s16x4 (&vhi)[8], f32x16 (&o)[2], float& l) {
;     const bf16x8 k00 = *(const LAS bf16x8*)(kp + ko0), k01 = *(const LAS bf16x8*)(kp + ko1), k10 = *(const LAS bf16x8*)(kp + ko0 + 4096), k11 = *(const LAS bf16x8*)(kp + ko1 + 4096);
;     f32x16 z;
; #pragma unroll
;     for (int i = 0; i < 16; ++i) z[i] = 0.f;
;     f32x16 s0 = FA_MFMA(k00, qf[0], z), s1 = FA_MFMA(k10, qf[0], z);
;     __builtin_amdgcn_sched_group_barrier(0x8, 2, 0);
;     s0 = FA_MFMA(k01, qf[1], s0); s1 = FA_MFMA(k11, qf[1], s1);
; #pragma unroll
;     for (int i = 0; i < 16; ++i) { s0[i] = __builtin_amdgcn_exp2f(s0[i]); s1[i] = __builtin_amdgcn_exp2f(s1[i]); }
;     float a = 0.f, b = 0.f;
; #pragma unroll
;     for (int i = 0; i < 16; ++i) { a += s0[i]; b += s1[i]; }
;     l += a + b;
;     u32x4 pw[4];
; #pragma unroll
;     for (int j = 0; j < 4; ++j) { pw[0][j] = cvtpk(s0[2 * j], s0[2 * j + 1]); pw[1][j] = cvtpk(s0[8 + 2 * j], s0[8 + 2 * j + 1]); pw[2][j] = cvtpk(s1[2 * j], s1[2 * j + 1]); pw[3][j] = cvtpk(s1[8 + 2 * j], s1[8 + 2 * j + 1]); }
; #pragma unroll
;     for (int ks = 0; ks < 4; ++ks)
; #pragma unroll
;         for (int d0 = 0; d0 < 2; ++d0) {
;             const int i = d0 * 4 + ks;
;             const bf16x8 vf = (bf16x8){vlo[i][0], vlo[i][1], vlo[i][2], vlo[i][3], vhi[i][0], vhi[i][1], vhi[i][2], vhi[i][3]};
;             o[d0] = FA_MFMA(__builtin_bit_cast(bf16x8, pw[ks]), vf, o[d0]);
;         }
; }
; template <class Mid> __device__ __forceinline__ void attn_unit(const Mid& mid, LAS unsigned char* lds, const bf16* __restrict__ Qu, const bf16* __restrict__ Kh, const bf16* __restrict__ Vh, int q0, int NT, ...
;     ...
;             const LAS unsigned char* kp = kp0 + sl + sb * SUBB; const LAS unsigned char* vp = vp0 + sl + sb * SUBB;
;             s16x4 vlo[8], vhi[8];
; #pragma unroll
;             for (int i = 0; i < 8; ++i) { vlo[i] = vtr(vp + (i >> 2) * 4096 + (i & 3) * 1024); vhi[i] = vtr(vp + (i >> 2) * 4096 + (i & 3) * 1024 + 512); }
;             map_tile(kp, ko10, ko11, q1f, vlo, vhi, o1, l1);
;             map_tile(kp, ko20, ko21, q2f, vlo, vhi, o2, l2);
	v_mfma_f32_32x32x16_bf16 v[66:81], v[164:167], v[140:143], 0
	ds_read_b128 v[164:167], v192 offset:16384
	v_exp_f32_e32 v105, v105
	v_cvt_pk_bf16_f32 v100, v102, v103
	v_cvt_pk_bf16_f32 v101, v104, v105
	v_exp_f32_e32 v106, v106
	v_exp_f32_e32 v107, v107
	v_mfma_f32_32x32x16_bf16 v[2:17], v[98:101], v[114:117], v[2:17]
	v_exp_f32_e32 v108, v108
	v_exp_f32_e32 v109, v109
	v_cvt_pk_bf16_f32 v102, v106, v107
	v_mfma_f32_32x32x16_bf16 v[18:33], v[98:101], v[184:187], v[18:33]
	v_cvt_pk_bf16_f32 v103, v108, v109
	v_exp_f32_e32 v110, v110
	v_exp_f32_e32 v111, v111
	v_mfma_f32_16x16x32_bf16 v[160:163], v[98:101], v[250:253], v[160:163]
	ds_read_b64_tr_b16 v[114:115], v220 offset:24576
	ds_read_b64_tr_b16 v[116:117], v220 offset:25088
	ds_read_b64_tr_b16 v[184:185], v220 offset:28672
	ds_read_b64_tr_b16 v[186:187], v220 offset:29184
	v_exp_f32_e32 v112, v112
	s_waitcnt lgkmcnt(7)
	v_mfma_f32_32x32x16_bf16 v[66:81], v[168:171], v[136:139], v[66:81]
	ds_read_b128 v[168:171], v193 offset:16384
	v_exp_f32_e32 v113, v113
	v_cvt_pk_bf16_f32 v104, v110, v111
	v_cvt_pk_bf16_f32 v105, v112, v113
	v_exp_f32_e32 v144, v144
	v_exp_f32_e32 v145, v145
	v_mfma_f32_32x32x16_bf16 v[2:17], v[102:105], v[118:121], v[2:17]
	v_exp_f32_e32 v146, v146
	v_exp_f32_e32 v147, v147
	v_cvt_pk_bf16_f32 v144, v144, v145
	v_mfma_f32_32x32x16_bf16 v[18:33], v[102:105], v[188:191], v[18:33]
	v_cvt_pk_bf16_f32 v145, v146, v147
	v_exp_f32_e32 v148, v148
	v_exp_f32_e32 v149, v149
	v_mfma_f32_16x16x32_bf16 v[160:163], v[102:105], v[250:253], v[160:163]
	ds_read_b64_tr_b16 v[118:119], v220 offset:25600
	ds_read_b64_tr_b16 v[120:121], v220 offset:26112
	ds_read_b64_tr_b16 v[188:189], v220 offset:29696
	ds_read_b64_tr_b16 v[190:191], v220 offset:30208
	v_exp_f32_e32 v150, v150
	s_waitcnt lgkmcnt(11)
	v_mfma_f32_32x32x16_bf16 v[82:97], v[172:175], v[140:143], 0
	ds_read_b128 v[172:175], v192 offset:20480
	v_exp_f32_e32 v151, v151
	v_cvt_pk_bf16_f32 v146, v148, v149
	v_cvt_pk_bf16_f32 v147, v150, v151
	v_exp_f32_e32 v152, v152
	v_exp_f32_e32 v153, v153
	v_mfma_f32_32x32x16_bf16 v[2:17], v[144:147], v[122:125], v[2:17]
	v_exp_f32_e32 v154, v154
	v_exp_f32_e32 v155, v155
	v_cvt_pk_bf16_f32 v148, v152, v153
	v_mfma_f32_32x32x16_bf16 v[18:33], v[144:147], v[222:225], v[18:33]
	v_cvt_pk_bf16_f32 v149, v154, v155
	v_exp_f32_e32 v156, v156
	v_exp_f32_e32 v157, v157
	v_mfma_f32_16x16x32_bf16 v[160:163], v[144:147], v[250:253], v[160:163]
	ds_read_b64_tr_b16 v[122:123], v220 offset:26624
	ds_read_b64_tr_b16 v[124:125], v220 offset:27136
	ds_read_b64_tr_b16 v[222:223], v220 offset:30720
	s_waitcnt lgkmcnt(14)
	ds_read_b64_tr_b16 v[224:225], v220 offset:31232
	v_exp_f32_e32 v158, v158
	v_mfma_f32_32x32x16_bf16 v[82:97], v[230:233], v[136:139], v[82:97]
	s_waitcnt lgkmcnt(14)
	ds_read_b128 v[230:233], v193 offset:20480
	v_exp_f32_e32 v159, v159
	v_cvt_pk_bf16_f32 v150, v156, v157
	v_cvt_pk_bf16_f32 v151, v158, v159
	v_exp_f32_e32 v66, v66
	v_exp_f32_e32 v67, v67
	v_mfma_f32_32x32x16_bf16 v[2:17], v[148:151], v[180:183], v[2:17]
	v_exp_f32_e32 v68, v68
	v_exp_f32_e32 v69, v69
	v_cvt_pk_bf16_f32 v66, v66, v67
	v_mfma_f32_32x32x16_bf16 v[18:33], v[148:151], v[226:229], v[18:33]
	v_cvt_pk_bf16_f32 v67, v68, v69
	v_exp_f32_e32 v70, v70
	v_exp_f32_e32 v71, v71
	v_mfma_f32_16x16x32_bf16 v[160:163], v[148:151], v[250:253], v[160:163]
	s_waitcnt lgkmcnt(14)
	ds_read_b64_tr_b16 v[180:181], v220 offset:27648
	s_waitcnt lgkmcnt(14)
	ds_read_b64_tr_b16 v[182:183], v220 offset:28160
	s_waitcnt lgkmcnt(14)
	ds_read_b64_tr_b16 v[226:227], v220 offset:31744
	s_waitcnt lgkmcnt(14)
	ds_read_b64_tr_b16 v[228:229], v220 offset:32256
	v_exp_f32_e32 v72, v72
	v_mfma_f32_32x32x16_bf16 v[98:113], v[164:167], v[132:135], 0
	v_exp_f32_e32 v73, v73
	v_cvt_pk_bf16_f32 v68, v70, v71
	v_cvt_pk_bf16_f32 v69, v72, v73
	v_exp_f32_e32 v74, v74
	v_exp_f32_e32 v75, v75
	v_mfma_f32_32x32x16_bf16 v[50:65], v[66:69], v[114:117], v[50:65]
	v_exp_f32_e32 v76, v76
	v_exp_f32_e32 v77, v77
	v_cvt_pk_bf16_f32 v70, v74, v75
	v_mfma_f32_32x32x16_bf16 v[34:49], v[66:69], v[184:187], v[34:49]
	v_cvt_pk_bf16_f32 v71, v76, v77
	v_exp_f32_e32 v78, v78
	v_exp_f32_e32 v79, v79
	v_mfma_f32_16x16x32_bf16 v[160:163], v[66:69], v[238:241], v[160:163]
	v_exp_f32_e32 v80, v80
	s_waitcnt lgkmcnt(14)
	v_mfma_f32_32x32x16_bf16 v[98:113], v[168:171], v[128:131], v[98:113]
	v_exp_f32_e32 v81, v81
	v_cvt_pk_bf16_f32 v72, v78, v79
	v_cvt_pk_bf16_f32 v73, v80, v81
	v_exp_f32_e32 v82, v82
	v_exp_f32_e32 v83, v83
	s_waitcnt lgkmcnt(12)
	v_mfma_f32_32x32x16_bf16 v[50:65], v[70:73], v[118:121], v[50:65]
	v_exp_f32_e32 v84, v84
	v_exp_f32_e32 v85, v85
	v_cvt_pk_bf16_f32 v82, v82, v83
	s_waitcnt lgkmcnt(10)
	v_mfma_f32_32x32x16_bf16 v[34:49], v[70:73], v[188:191], v[34:49]
	v_cvt_pk_bf16_f32 v83, v84, v85
	v_exp_f32_e32 v86, v86
	v_exp_f32_e32 v87, v87
	v_mfma_f32_16x16x32_bf16 v[160:163], v[70:73], v[238:241], v[160:163]
	v_exp_f32_e32 v88, v88
	s_waitcnt lgkmcnt(9)
	v_mfma_f32_32x32x16_bf16 v[144:159], v[172:175], v[132:135], 0
	v_exp_f32_e32 v89, v89
	v_cvt_pk_bf16_f32 v84, v86, v87
	v_cvt_pk_bf16_f32 v85, v88, v89
	v_exp_f32_e32 v90, v90
	v_exp_f32_e32 v91, v91
	s_waitcnt lgkmcnt(7)
	v_mfma_f32_32x32x16_bf16 v[50:65], v[82:85], v[122:125], v[50:65]
	v_exp_f32_e32 v92, v92
	v_exp_f32_e32 v93, v93
	v_cvt_pk_bf16_f32 v86, v90, v91
	s_waitcnt lgkmcnt(5)
	v_mfma_f32_32x32x16_bf16 v[34:49], v[82:85], v[222:225], v[34:49]
	v_cvt_pk_bf16_f32 v87, v92, v93
	v_exp_f32_e32 v94, v94
	v_exp_f32_e32 v95, v95
	v_mfma_f32_16x16x32_bf16 v[160:163], v[82:85], v[238:241], v[160:163]
	v_exp_f32_e32 v96, v96
	s_waitcnt lgkmcnt(4)
; #define LAS __attribute__((address_space(3)))
; #define FA_MFMA(a, b, c) __builtin_amdgcn_mfma_f32_32x32x16_bf16((a), (b), (c), 0, 0, 0)
; __device__ __forceinline__ void map_tile(const LAS unsigned char* kp, int ko0, int ko1, const bf16x8 (&qf)[2], const s16x4 (&vlo)[8], const s16x4 (&vhi)[8], f32x16 (&o)[2], float& l) {
;     const bf16x8 k00 = *(const LAS bf16x8*)(kp + ko0), k01 = *(const LAS bf16x8*)(kp + ko1), k10 = *(const LAS bf16x8*)(kp + ko0 + 4096), k11 = *(const LAS bf16x8*)(kp + ko1 + 4096);
;     f32x16 z;
; #pragma unroll
;     for (int i = 0; i < 16; ++i) z[i] = 0.f;
;     f32x16 s0 = FA_MFMA(k00, qf[0], z), s1 = FA_MFMA(k10, qf[0], z);
;     __builtin_amdgcn_sched_group_barrier(0x8, 2, 0);
;     s0 = FA_MFMA(k01, qf[1], s0); s1 = FA_MFMA(k11, qf[1], s1);
; #pragma unroll
;     for (int i = 0; i < 16; ++i) { s0[i] = __builtin_amdgcn_exp2f(s0[i]); s1[i] = __builtin_amdgcn_exp2f(s1[i]); }
;     float a = 0.f, b = 0.f;
; #pragma unroll
;     for (int i = 0; i < 16; ++i) { a += s0[i]; b += s1[i]; }
;     l += a + b;
;     u32x4 pw[4];
; #pragma unroll
;     for (int j = 0; j < 4; ++j) { pw[0][j] = cvtpk(s0[2 * j], s0[2 * j + 1]); pw[1][j] = cvtpk(s0[8 + 2 * j], s0[8 + 2 * j + 1]); pw[2][j] = cvtpk(s1[2 * j], s1[2 * j + 1]); pw[3][j] = cvtpk(s1[8 + 2 * j], s1[8 + 2 * j + 1]); }
; #pragma unroll
;     for (int ks = 0; ks < 4; ++ks)
; #pragma unroll
;         for (int d0 = 0; d0 < 2; ++d0) {
;             const int i = d0 * 4 + ks;
;             const bf16x8 vf = (bf16x8){vlo[i][0], vlo[i][1], vlo[i][2], vlo[i][3], vhi[i][0], vhi[i][1], vhi[i][2], vhi[i][3]};
;             o[d0] = FA_MFMA(__builtin_bit_cast(bf16x8, pw[ks]), vf, o[d0]);
;         }
; }
; template <class Mid> __device__ __forceinline__ void attn_unit(const Mid& mid, LAS unsigned char* lds, const bf16* __restrict__ Qu, const bf16* __restrict__ Kh, const bf16* __restrict__ Vh, int q0, int NT, ...
;     ...
;     asm volatile("s_waitcnt vmcnt(0) lgkmcnt(0)\n\ts_barrier" ::: "memory");
;     f32x4 xv[32]; mid.load(xv);
;     l1 += __shfl_xor(l1, 32); l2 += __shfl_xor(l2, 32);
;     int lane_e = lane; asm volatile("" : "+v"(lane_e));
;     const int r32e = lane_e & 31, hie = lane_e >> 5;
;     LAS float* wsf = (LAS float*)(lds + FA_WS) + wid * 64;
;     if (hie == 0) { wsf[r32e] = 1.0f / l1; wsf[32 + r32e] = lam / l2; }
	v_mfma_f32_32x32x16_bf16 v[144:159], v[230:233], v[128:131], v[144:159]
	v_exp_f32_e32 v97, v97
	v_cvt_pk_bf16_f32 v88, v94, v95
	v_cvt_pk_bf16_f32 v89, v96, v97
	v_exp_f32_e32 v98, v98
	v_exp_f32_e32 v99, v99
	s_waitcnt lgkmcnt(2)
	v_mfma_f32_32x32x16_bf16 v[50:65], v[86:89], v[180:183], v[50:65]
	v_exp_f32_e32 v100, v100
	v_exp_f32_e32 v101, v101
	v_cvt_pk_bf16_f32 v98, v98, v99
	s_waitcnt lgkmcnt(0)
	v_mfma_f32_32x32x16_bf16 v[34:49], v[86:89], v[226:229], v[34:49]
	v_cvt_pk_bf16_f32 v99, v100, v101
	v_exp_f32_e32 v102, v102
	v_exp_f32_e32 v103, v103
	v_mfma_f32_16x16x32_bf16 v[160:163], v[86:89], v[238:241], v[160:163]
	v_exp_f32_e32 v104, v104
	v_exp_f32_e32 v105, v105
	v_cvt_pk_bf16_f32 v100, v102, v103
	v_cvt_pk_bf16_f32 v101, v104, v105
	v_exp_f32_e32 v106, v106
	v_exp_f32_e32 v107, v107
	v_mfma_f32_32x32x16_bf16 v[2:17], v[98:101], v[114:117], v[2:17]
	v_exp_f32_e32 v108, v108
	v_exp_f32_e32 v109, v109
	v_cvt_pk_bf16_f32 v102, v106, v107
	v_mfma_f32_32x32x16_bf16 v[18:33], v[98:101], v[184:187], v[18:33]
	v_cvt_pk_bf16_f32 v103, v108, v109
	v_exp_f32_e32 v110, v110
	v_exp_f32_e32 v111, v111
	v_mfma_f32_16x16x32_bf16 v[160:163], v[98:101], v[250:253], v[160:163]
	v_exp_f32_e32 v112, v112
	v_exp_f32_e32 v113, v113
	v_cvt_pk_bf16_f32 v104, v110, v111
	v_cvt_pk_bf16_f32 v105, v112, v113
	v_exp_f32_e32 v144, v144
	v_exp_f32_e32 v145, v145
	v_mfma_f32_32x32x16_bf16 v[2:17], v[102:105], v[118:121], v[2:17]
	v_exp_f32_e32 v146, v146
	v_exp_f32_e32 v147, v147
	v_cvt_pk_bf16_f32 v144, v144, v145
	v_mfma_f32_32x32x16_bf16 v[18:33], v[102:105], v[188:191], v[18:33]
	v_cvt_pk_bf16_f32 v145, v146, v147
	v_exp_f32_e32 v148, v148
	v_exp_f32_e32 v149, v149
	v_mfma_f32_16x16x32_bf16 v[160:163], v[102:105], v[250:253], v[160:163]
	v_exp_f32_e32 v150, v150
	v_exp_f32_e32 v151, v151
	v_cvt_pk_bf16_f32 v146, v148, v149
	v_cvt_pk_bf16_f32 v147, v150, v151
	v_exp_f32_e32 v152, v152
	v_exp_f32_e32 v153, v153
	v_mfma_f32_32x32x16_bf16 v[2:17], v[144:147], v[122:125], v[2:17]
	v_exp_f32_e32 v154, v154
	v_exp_f32_e32 v155, v155
	v_cvt_pk_bf16_f32 v148, v152, v153
	v_mfma_f32_32x32x16_bf16 v[18:33], v[144:147], v[222:225], v[18:33]
	v_cvt_pk_bf16_f32 v149, v154, v155
	v_exp_f32_e32 v156, v156
	v_exp_f32_e32 v157, v157
	v_mfma_f32_16x16x32_bf16 v[160:163], v[144:147], v[250:253], v[160:163]
	v_exp_f32_e32 v158, v158
	v_exp_f32_e32 v159, v159
	v_cvt_pk_bf16_f32 v150, v156, v157
	v_cvt_pk_bf16_f32 v151, v158, v159
	s_nop 1
	v_mfma_f32_32x32x16_bf16 v[2:17], v[148:151], v[180:183], v[2:17]
	v_mfma_f32_32x32x16_bf16 v[18:33], v[148:151], v[226:229], v[18:33]
	v_mfma_f32_16x16x32_bf16 v[160:163], v[148:151], v[250:253], v[160:163]
	s_add_i32 s14, s72, 0x8000
	s_cmp_lt_i32 s72, 0x10000
	s_cselect_b32 s72, s14, 0
	s_add_i32 s73, s73, 1
	s_cmp_eq_u32 s73, s68
	s_cbranch_scc0 .LBB0_460
	s_nop 15
	v_readfirstlane_b32 s100, v0
	v_mbcnt_lo_u32_b32 v198, -1, 0
	v_mbcnt_hi_u32_b32 v198, -1, v198
	s_and_b32 s100, s100, 0x1c0
	s_lshl_b32 s100, s100, 2
	s_add_i32 s100, s100, 0x20000
	v_and_b32_e32 v199, 15, v198
	v_lshrrev_b32_e32 v202, 4, v198
	v_lshlrev_b32_e32 v203, 6, v199
	v_lshl_add_u32 v203, v202, 4, v203
	v_add_u32_e32 v203, s100, v203
	v_and_b32_e32 v199, 31, v198
	v_lshl_add_u32 v202, v199, 2, s100
	s_mov_b64 s[98:99], exec
	s_mov_b32 exec_lo, 0xf000f
	s_mov_b32 exec_hi, 0xf000f
	ds_write_b128 v203, v[160:163]
	s_mov_b64 exec, s[98:99]
	s_waitcnt lgkmcnt(0)
	ds_read_b32 v201, v202
	ds_read_b32 v200, v202 offset:128
	s_waitcnt lgkmcnt(0)
	v_mul_f32_e32 v200, 0.5, v200
	v_mul_f32_e32 v201, 0.5, v201
	s_lshl_b32 s28, s69, 6
	s_lshl_b32 s14, s54, 5
	s_and_b32 s49, s28, 0x3c0
	s_cmpk_lt_i32 s54, 0x3000
	s_cselect_b64 s[28:29], -1, 0
	s_and_b32 s14, s14, 32
	s_waitcnt vmcnt(0) lgkmcnt(0)
	s_barrier
	s_or_b32 s14, s49, s14
	s_cmpk_gt_i32 s54, 0x2fff
	v_or_b32_e32 v198, s67, v209
	s_cbranch_scc1 .LBB0_465
	s_mul_i32 s49, s34, s14
	s_lshl_b32 s49, s49, 2
	s_add_u32 s68, s30, s49
	s_addc_u32 s69, s31, 0
	s_or_b32 s49, s14, 1
	v_mov_b32_e32 v199, v197
	s_mul_i32 s49, s34, s49
	v_lshlrev_b64 v[186:187], 2, v[198:199]
	s_lshl_b32 s49, s49, 2
	v_lshl_add_u64 v[66:67], s[68:69], 0, v[186:187]
	s_add_u32 s68, s30, s49
	s_addc_u32 s69, s31, 0
	s_or_b32 s49, s14, 2
	s_mul_i32 s49, s34, s49
	s_lshl_b32 s49, s49, 2
	v_lshl_add_u64 v[68:69], s[68:69], 0, v[186:187]
	s_add_u32 s68, s30, s49
	s_addc_u32 s69, s31, 0
	s_or_b32 s49, s14, 3
	s_mul_i32 s49, s34, s49
	s_lshl_b32 s49, s49, 2
	v_lshl_add_u64 v[74:75], s[68:69], 0, v[186:187]
	s_add_u32 s68, s30, s49
	s_addc_u32 s69, s31, 0
	s_or_b32 s49, s14, 4
	s_mul_i32 s49, s34, s49
	s_lshl_b32 s49, s49, 2
	v_lshl_add_u64 v[76:77], s[68:69], 0, v[186:187]
	s_add_u32 s68, s30, s49
	s_addc_u32 s69, s31, 0
	s_or_b32 s49, s14, 5
	s_mul_i32 s49, s34, s49
	s_lshl_b32 s49, s49, 2
	v_lshl_add_u64 v[82:83], s[68:69], 0, v[186:187]
	s_add_u32 s68, s30, s49
	s_addc_u32 s69, s31, 0
	s_or_b32 s49, s14, 6
	s_mul_i32 s49, s34, s49
	s_lshl_b32 s49, s49, 2
	v_lshl_add_u64 v[84:85], s[68:69], 0, v[186:187]
	s_add_u32 s68, s30, s49
	s_addc_u32 s69, s31, 0
	s_or_b32 s49, s14, 7
	s_mul_i32 s49, s34, s49
	s_lshl_b32 s49, s49, 2
	v_lshl_add_u64 v[90:91], s[68:69], 0, v[186:187]
	s_add_u32 s68, s30, s49
	s_addc_u32 s69, s31, 0
	s_or_b32 s49, s14, 8
	s_mul_i32 s49, s34, s49
	s_lshl_b32 s49, s49, 2
	v_lshl_add_u64 v[92:93], s[68:69], 0, v[186:187]
	s_add_u32 s68, s30, s49
	s_addc_u32 s69, s31, 0
	s_or_b32 s49, s14, 9
	s_mul_i32 s49, s34, s49
	s_lshl_b32 s49, s49, 2
	v_lshl_add_u64 v[98:99], s[68:69], 0, v[186:187]
	s_add_u32 s68, s30, s49
	s_addc_u32 s69, s31, 0
	s_or_b32 s49, s14, 10
	s_mul_i32 s49, s34, s49
	s_lshl_b32 s49, s49, 2
;     __device__ __forceinline__ void load(f32x4 (&v)[32]) const { if (on) {
; #pragma unroll
;         for (int i = 0; i < 32; ++i) v[i] = *(const f32x4*)(src + (size_t)(k0 + i) * N + n0); } }
	v_lshl_add_u64 v[100:101], s[68:69], 0, v[186:187]
	s_add_u32 s68, s30, s49
	s_addc_u32 s69, s31, 0
	s_or_b32 s49, s14, 11
	s_mul_i32 s49, s34, s49
	s_lshl_b32 s49, s49, 2
	v_lshl_add_u64 v[106:107], s[68:69], 0, v[186:187]
	s_add_u32 s68, s30, s49
	s_addc_u32 s69, s31, 0
	s_or_b32 s49, s14, 12
	s_mul_i32 s49, s34, s49
	s_lshl_b32 s49, s49, 2
	v_lshl_add_u64 v[108:109], s[68:69], 0, v[186:187]
	s_add_u32 s68, s30, s49
	s_addc_u32 s69, s31, 0
	s_or_b32 s49, s14, 13
	s_mul_i32 s49, s34, s49
	s_lshl_b32 s49, s49, 2
	v_lshl_add_u64 v[114:115], s[68:69], 0, v[186:187]
	s_add_u32 s68, s30, s49
	s_addc_u32 s69, s31, 0
	s_or_b32 s49, s14, 14
	s_mul_i32 s49, s34, s49
	s_lshl_b32 s49, s49, 2
	v_lshl_add_u64 v[116:117], s[68:69], 0, v[186:187]
	s_add_u32 s68, s30, s49
	s_addc_u32 s69, s31, 0
	s_or_b32 s49, s14, 15
	s_mul_i32 s49, s34, s49
	s_lshl_b32 s49, s49, 2
	v_lshl_add_u64 v[122:123], s[68:69], 0, v[186:187]
	s_add_u32 s68, s30, s49
	s_addc_u32 s69, s31, 0
	s_or_b32 s49, s14, 16
	s_mul_i32 s49, s34, s49
	s_lshl_b32 s49, s49, 2
	v_lshl_add_u64 v[124:125], s[68:69], 0, v[186:187]
	s_add_u32 s68, s30, s49
	s_addc_u32 s69, s31, 0
	s_or_b32 s49, s14, 17
	s_mul_i32 s49, s34, s49
	s_lshl_b32 s49, s49, 2
	v_lshl_add_u64 v[126:127], s[68:69], 0, v[186:187]
	s_add_u32 s68, s30, s49
	s_addc_u32 s69, s31, 0
	s_or_b32 s49, s14, 18
	s_mul_i32 s49, s34, s49
	s_lshl_b32 s49, s49, 2
	v_lshl_add_u64 v[128:129], s[68:69], 0, v[186:187]
	s_add_u32 s68, s30, s49
	s_addc_u32 s69, s31, 0
	s_or_b32 s49, s14, 19
	s_mul_i32 s49, s34, s49
	s_lshl_b32 s49, s49, 2
	v_lshl_add_u64 v[138:139], s[68:69], 0, v[186:187]
	s_add_u32 s68, s30, s49
	s_addc_u32 s69, s31, 0
	s_or_b32 s49, s14, 20
	s_mul_i32 s49, s34, s49
	s_lshl_b32 s49, s49, 2
	v_lshl_add_u64 v[140:141], s[68:69], 0, v[186:187]
	s_add_u32 s68, s30, s49
	s_addc_u32 s69, s31, 0
	s_or_b32 s49, s14, 21
	s_mul_i32 s49, s34, s49
	s_lshl_b32 s49, s49, 2
	v_lshl_add_u64 v[146:147], s[68:69], 0, v[186:187]
	s_add_u32 s68, s30, s49
	s_addc_u32 s69, s31, 0
	s_or_b32 s49, s14, 22
	s_mul_i32 s49, s34, s49
	s_lshl_b32 s49, s49, 2
	v_lshl_add_u64 v[148:149], s[68:69], 0, v[186:187]
	s_add_u32 s68, s30, s49
	s_addc_u32 s69, s31, 0
	s_or_b32 s49, s14, 23
	s_mul_i32 s49, s34, s49
	s_lshl_b32 s49, s49, 2
	v_lshl_add_u64 v[154:155], s[68:69], 0, v[186:187]
	s_add_u32 s68, s30, s49
	s_addc_u32 s69, s31, 0
	s_or_b32 s49, s14, 24
	s_mul_i32 s49, s34, s49
	s_lshl_b32 s49, s49, 2
	v_lshl_add_u64 v[156:157], s[68:69], 0, v[186:187]
	s_add_u32 s68, s30, s49
	s_addc_u32 s69, s31, 0
	s_or_b32 s49, s14, 25
	s_mul_i32 s49, s34, s49
	s_lshl_b32 s49, s49, 2
	v_lshl_add_u64 v[162:163], s[68:69], 0, v[186:187]
	s_add_u32 s68, s30, s49
	s_addc_u32 s69, s31, 0
	s_or_b32 s49, s14, 26
	s_mul_i32 s49, s34, s49
	s_lshl_b32 s49, s49, 2
	v_lshl_add_u64 v[164:165], s[68:69], 0, v[186:187]
	s_add_u32 s68, s30, s49
	s_addc_u32 s69, s31, 0
	s_or_b32 s49, s14, 27
	s_mul_i32 s49, s34, s49
	s_lshl_b32 s49, s49, 2
	v_lshl_add_u64 v[170:171], s[68:69], 0, v[186:187]
	s_add_u32 s68, s30, s49
	s_addc_u32 s69, s31, 0
	s_or_b32 s49, s14, 28
	s_mul_i32 s49, s34, s49
	s_lshl_b32 s49, s49, 2
	v_lshl_add_u64 v[172:173], s[68:69], 0, v[186:187]
	s_add_u32 s68, s30, s49
	s_addc_u32 s69, s31, 0
	s_or_b32 s49, s14, 29
	s_mul_i32 s49, s34, s49
	s_lshl_b32 s49, s49, 2
	v_lshl_add_u64 v[178:179], s[68:69], 0, v[186:187]
	s_add_u32 s68, s30, s49
	s_addc_u32 s69, s31, 0
	s_or_b32 s49, s14, 30
	s_mul_i32 s49, s34, s49
	s_lshl_b32 s49, s49, 2
	v_lshl_add_u64 v[180:181], s[68:69], 0, v[186:187]
	s_add_u32 s68, s30, s49
	s_addc_u32 s69, s31, 0
	s_or_b32 s49, s14, 31
	s_mul_i32 s34, s34, s49
	s_lshl_b32 s34, s34, 2
	s_add_u32 s30, s30, s34
	s_addc_u32 s31, s31, 0
	v_lshl_add_u64 v[188:189], s[68:69], 0, v[186:187]
	v_lshl_add_u64 v[186:187], s[30:31], 0, v[186:187]
	global_load_dwordx4 v[70:73], v[66:67], off
	s_nop 0
	global_load_dwordx4 v[66:69], v[68:69], off
	s_nop 0
	global_load_dwordx4 v[78:81], v[74:75], off
	s_nop 0
	global_load_dwordx4 v[74:77], v[76:77], off
	s_nop 0
	global_load_dwordx4 v[86:89], v[82:83], off
	s_nop 0
	global_load_dwordx4 v[82:85], v[84:85], off
	s_nop 0
	global_load_dwordx4 v[94:97], v[90:91], off
	s_nop 0
	global_load_dwordx4 v[90:93], v[92:93], off
	s_nop 0
	global_load_dwordx4 v[102:105], v[98:99], off
	s_nop 0
	global_load_dwordx4 v[98:101], v[100:101], off
	s_nop 0
	global_load_dwordx4 v[110:113], v[106:107], off
	s_nop 0
	global_load_dwordx4 v[106:109], v[108:109], off
	s_nop 0
	global_load_dwordx4 v[118:121], v[114:115], off
	s_nop 0
	global_load_dwordx4 v[114:117], v[116:117], off
	s_nop 0
	global_load_dwordx4 v[130:133], v[122:123], off
	s_nop 0
	global_load_dwordx4 v[122:125], v[124:125], off
	s_nop 0
	global_load_dwordx4 v[134:137], v[126:127], off
	s_nop 0
	global_load_dwordx4 v[126:129], v[128:129], off
	s_nop 0
	global_load_dwordx4 v[142:145], v[138:139], off
	s_nop 0
	global_load_dwordx4 v[138:141], v[140:141], off
	s_nop 0
	global_load_dwordx4 v[150:153], v[146:147], off
	s_nop 0
	global_load_dwordx4 v[146:149], v[148:149], off
	s_nop 0
	global_load_dwordx4 v[158:161], v[154:155], off
	s_nop 0
	global_load_dwordx4 v[154:157], v[156:157], off
	s_nop 0
	global_load_dwordx4 v[166:169], v[162:163], off
	s_nop 0
	global_load_dwordx4 v[162:165], v[164:165], off
	s_nop 0
	global_load_dwordx4 v[174:177], v[170:171], off
	s_nop 0
	global_load_dwordx4 v[170:173], v[172:173], off
	s_nop 0
	global_load_dwordx4 v[182:185], v[178:179], off
	s_nop 0
	global_load_dwordx4 v[178:181], v[180:181], off
	s_nop 0
	global_load_dwordx4 v[190:193], v[188:189], off
	s_nop 0
	global_load_dwordx4 v[186:189], v[186:187], off

; #define LAS __attribute__((address_space(3)))
; __device__ __forceinline__ void map_tile(const LAS unsigned char* kp, int ko0, int ko1, const bf16x8 (&qf)[2], const s16x4 (&vlo)[8], const s16x4 (&vhi)[8], f32x16 (&o)[2], float& l) {
;     const bf16x8 k00 = *(const LAS bf16x8*)(kp + ko0), k01 = *(const LAS bf16x8*)(kp + ko1), k10 = *(const LAS bf16x8*)(kp + ko0 + 4096), k11 = *(const LAS bf16x8*)(kp + ko1 + 4096);
;     f32x16 z;
; #pragma unroll
;     for (int i = 0; i < 16; ++i) z[i] = 0.f;
;     f32x16 s0 = FA_MFMA(k00, qf[0], z), s1 = FA_MFMA(k10, qf[0], z);
;     __builtin_amdgcn_sched_group_barrier(0x8, 2, 0);
;     s0 = FA_MFMA(k01, qf[1], s0); s1 = FA_MFMA(k11, qf[1], s1);
; #pragma unroll
;     for (int i = 0; i < 16; ++i) { s0[i] = __builtin_amdgcn_exp2f(s0[i]); s1[i] = __builtin_amdgcn_exp2f(s1[i]); }
;     float a = 0.f, b = 0.f;
; #pragma unroll
;     for (int i = 0; i < 16; ++i) { a += s0[i]; b += s1[i]; }
;     l += a + b;
;     u32x4 pw[4];
; #pragma unroll
;     for (int j = 0; j < 4; ++j) { pw[0][j] = cvtpk(s0[2 * j], s0[2 * j + 1]); pw[1][j] = cvtpk(s0[8 + 2 * j], s0[8 + 2 * j + 1]); pw[2][j] = cvtpk(s1[2 * j], s1[2 * j + 1]); pw[3][j] = cvtpk(s1[8 + 2 * j], s1[8 + 2 * j + 1]); }
; #pragma unroll
;     for (int ks = 0; ks < 4; ++ks)
; #pragma unroll
;         for (int d0 = 0; d0 < 2; ++d0) {
;             const int i = d0 * 4 + ks;
; template <class Mid> __device__ __forceinline__ void attn_unit(const Mid& mid, LAS unsigned char* lds, const bf16* __restrict__ Qu, const bf16* __restrict__ Kh, const bf16* __restrict__ Vh, int q0, int NT, ...
;     ...
;     for (int t = 0; t < NT2; ++t) {
;         FA_WAIT_BAR(4);
;         { const int tn = (t + PFD < NT2) ? t + PFD : NT2 - 1; const int sn = (sl == 0) ? (NSLOT - 1) * SLOTB : sl - SLOTB; FA_DMA(tn, sn); }
; #pragma unroll 1
;         for (int sb = 0; sb < 2; ++sb) {
;             const LAS unsigned char* kp = kp0 + sl + sb * SUBB; const LAS unsigned char* vp = vp0 + sl + sb * SUBB;
;             s16x4 vlo[8], vhi[8];
; #pragma unroll
;             for (int i = 0; i < 8; ++i) { vlo[i] = vtr(vp + (i >> 2) * 4096 + (i & 3) * 1024); vhi[i] = vtr(vp + (i >> 2) * 4096 + (i & 3) * 1024 + 512); }
;             map_tile(kp, ko10, ko11, q1f, vlo, vhi, o1, l1);
;             map_tile(kp, ko20, ko21, q2f, vlo, vhi, o2, l2);
;             __builtin_amdgcn_sched_barrier(0);
;         }
.LBB0_1357:
	s_min_u32 s12, s71, 31
	s_add_i32 s24, s70, 0xffff8000
	s_cmp_lg_u32 s70, 0
	s_cselect_b32 s24, s24, 0x10000
	s_lshl_b32 s72, s12, 14
	s_waitcnt vmcnt(4) lgkmcnt(0)
	s_barrier
	v_add_u32_e32 v196, s70, v214
	v_add_u32_e32 v220, s70, v219
	v_add_u32_e32 v126, v196, v215
	v_add_u32_e32 v127, v196, v217
	v_add_u32_e32 v192, v196, v216
	v_add_u32_e32 v193, v196, v218
	ds_read_b128 v[164:167], v126
	ds_read_b128 v[168:171], v127
	ds_read_b128 v[172:175], v126 offset:4096
	ds_read_b128 v[230:233], v127 offset:4096
	ds_read_b64_tr_b16 v[114:115], v220 offset:8192
	ds_read_b64_tr_b16 v[116:117], v220 offset:8704
	ds_read_b64_tr_b16 v[184:185], v220 offset:12288
	ds_read_b64_tr_b16 v[186:187], v220 offset:12800
	s_add_i32 s12, s72, 0x8000
	s_add_i32 s25, s24, s68
	v_lshl_add_u64 v[66:67], v[176:177], 0, s[12:13]
	s_mov_b32 s73, m0
	s_mov_b32 m0, s25
	s_nop 0
	global_load_lds_dwordx4 v[66:67], off
	s_mov_b32 m0, s73
	s_add_i32 s24, s24, s69
	v_lshl_add_u64 v[66:67], v[178:179], 0, s[12:13]
	s_mov_b32 s12, m0
	s_mov_b32 m0, s24
	s_nop 0
	global_load_lds_dwordx4 v[66:67], off
	s_mov_b32 m0, s12
	s_add_i32 s12, s72, 0xa000
	v_lshl_add_u64 v[66:67], v[176:177], 0, s[12:13]
	s_addk_i32 s25, 0x4000
	s_mov_b32 s72, m0
	s_mov_b32 m0, s25
	s_nop 0
	global_load_lds_dwordx4 v[66:67], off
	s_mov_b32 m0, s72
	v_lshl_add_u64 v[66:67], v[178:179], 0, s[12:13]
	s_add_i32 s12, s24, 0x4000
	s_mov_b32 s24, m0
	s_mov_b32 m0, s12
	s_nop 0
	global_load_lds_dwordx4 v[66:67], off
	s_mov_b32 m0, s24
	s_waitcnt lgkmcnt(7)
	v_mfma_f32_32x32x16_bf16 v[66:81], v[164:167], v[140:143], 0
	ds_read_b128 v[164:167], v192
	s_waitcnt lgkmcnt(7)
	v_mfma_f32_32x32x16_bf16 v[66:81], v[168:171], v[136:139], v[66:81]
	ds_read_b128 v[168:171], v193
	ds_read_b64_tr_b16 v[118:119], v220 offset:9216
	ds_read_b64_tr_b16 v[120:121], v220 offset:9728
	ds_read_b64_tr_b16 v[188:189], v220 offset:13312
	ds_read_b64_tr_b16 v[190:191], v220 offset:13824
	s_waitcnt lgkmcnt(11)
	v_mfma_f32_32x32x16_bf16 v[82:97], v[172:175], v[140:143], 0
	ds_read_b128 v[172:175], v192 offset:4096
	s_waitcnt lgkmcnt(11)
	v_mfma_f32_32x32x16_bf16 v[82:97], v[230:233], v[136:139], v[82:97]
	ds_read_b128 v[230:233], v193 offset:4096
	ds_read_b64_tr_b16 v[122:123], v220 offset:10240
	ds_read_b64_tr_b16 v[124:125], v220 offset:10752
	ds_read_b64_tr_b16 v[222:223], v220 offset:14336
	s_waitcnt lgkmcnt(14)
	ds_read_b64_tr_b16 v[224:225], v220 offset:14848
	s_nop 1
	s_waitcnt lgkmcnt(14)
	ds_read_b64_tr_b16 v[180:181], v220 offset:11264
	s_waitcnt lgkmcnt(14)
	ds_read_b64_tr_b16 v[182:183], v220 offset:11776
	s_waitcnt lgkmcnt(14)
	ds_read_b64_tr_b16 v[226:227], v220 offset:15360
	s_waitcnt lgkmcnt(14)
	ds_read_b64_tr_b16 v[228:229], v220 offset:15872
	v_exp_f32_e32 v66, v66
	v_exp_f32_e32 v67, v67
	v_exp_f32_e32 v68, v68
	v_exp_f32_e32 v69, v69
	v_cvt_pk_bf16_f32 v66, v66, v67
	v_cvt_pk_bf16_f32 v67, v68, v69
	v_exp_f32_e32 v70, v70
	v_exp_f32_e32 v71, v71
	v_exp_f32_e32 v72, v72
	v_mfma_f32_32x32x16_bf16 v[98:113], v[164:167], v[132:135], 0
	s_waitcnt lgkmcnt(14)
	ds_read_b128 v[164:167], v126 offset:16384
	v_exp_f32_e32 v73, v73
	v_cvt_pk_bf16_f32 v68, v70, v71
	v_cvt_pk_bf16_f32 v69, v72, v73
	v_exp_f32_e32 v74, v74
	v_exp_f32_e32 v75, v75
	v_mfma_f32_32x32x16_bf16 v[50:65], v[66:69], v[114:117], v[50:65]
	v_exp_f32_e32 v76, v76
	v_exp_f32_e32 v77, v77
	v_cvt_pk_bf16_f32 v70, v74, v75
	v_mfma_f32_32x32x16_bf16 v[34:49], v[66:69], v[184:187], v[34:49]
	v_cvt_pk_bf16_f32 v71, v76, v77
	v_exp_f32_e32 v78, v78
	v_exp_f32_e32 v79, v79
	v_mfma_f32_16x16x32_bf16 v[160:163], v[66:69], v[238:241], v[160:163]
	v_exp_f32_e32 v80, v80
	v_mfma_f32_32x32x16_bf16 v[98:113], v[168:171], v[128:131], v[98:113]
	s_waitcnt lgkmcnt(14)
	ds_read_b128 v[168:171], v127 offset:16384
	v_exp_f32_e32 v81, v81
	v_cvt_pk_bf16_f32 v72, v78, v79
	v_cvt_pk_bf16_f32 v73, v80, v81
	v_exp_f32_e32 v82, v82
	v_exp_f32_e32 v83, v83
	s_waitcnt lgkmcnt(14)
	v_mfma_f32_32x32x16_bf16 v[50:65], v[70:73], v[118:121], v[50:65]
	v_exp_f32_e32 v84, v84
	v_exp_f32_e32 v85, v85
	v_cvt_pk_bf16_f32 v82, v82, v83
	s_waitcnt lgkmcnt(12)
	v_mfma_f32_32x32x16_bf16 v[34:49], v[70:73], v[188:191], v[34:49]
	v_cvt_pk_bf16_f32 v83, v84, v85
	v_exp_f32_e32 v86, v86
	v_exp_f32_e32 v87, v87
	v_mfma_f32_16x16x32_bf16 v[160:163], v[70:73], v[238:241], v[160:163]
	v_exp_f32_e32 v88, v88
	s_waitcnt lgkmcnt(11)
	v_mfma_f32_32x32x16_bf16 v[144:159], v[172:175], v[132:135], 0
	ds_read_b128 v[172:175], v126 offset:20480
	v_exp_f32_e32 v89, v89
	v_cvt_pk_bf16_f32 v84, v86, v87
	v_cvt_pk_bf16_f32 v85, v88, v89
	v_exp_f32_e32 v90, v90
	v_exp_f32_e32 v91, v91
	s_waitcnt lgkmcnt(9)
	v_mfma_f32_32x32x16_bf16 v[50:65], v[82:85], v[122:125], v[50:65]
	v_exp_f32_e32 v92, v92
	v_exp_f32_e32 v93, v93
	v_cvt_pk_bf16_f32 v86, v90, v91
	s_waitcnt lgkmcnt(7)
	v_mfma_f32_32x32x16_bf16 v[34:49], v[82:85], v[222:225], v[34:49]
	v_cvt_pk_bf16_f32 v87, v92, v93
	v_exp_f32_e32 v94, v94
	v_exp_f32_e32 v95, v95
	v_mfma_f32_16x16x32_bf16 v[160:163], v[82:85], v[238:241], v[160:163]
	v_exp_f32_e32 v96, v96
	v_mfma_f32_32x32x16_bf16 v[144:159], v[230:233], v[128:131], v[144:159]
	ds_read_b128 v[230:233], v127 offset:20480
	v_exp_f32_e32 v97, v97
	v_cvt_pk_bf16_f32 v88, v94, v95
	v_cvt_pk_bf16_f32 v89, v96, v97
	v_exp_f32_e32 v98, v98
	v_exp_f32_e32 v99, v99
	s_waitcnt lgkmcnt(6)
	v_mfma_f32_32x32x16_bf16 v[50:65], v[86:89], v[180:183], v[50:65]
	v_exp_f32_e32 v100, v100
	v_exp_f32_e32 v101, v101
	v_cvt_pk_bf16_f32 v98, v98, v99
	s_waitcnt lgkmcnt(4)
	v_mfma_f32_32x32x16_bf16 v[34:49], v[86:89], v[226:229], v[34:49]
	v_cvt_pk_bf16_f32 v99, v100, v101
	v_exp_f32_e32 v102, v102
	v_exp_f32_e32 v103, v103
	v_mfma_f32_16x16x32_bf16 v[160:163], v[86:89], v[238:241], v[160:163]
	v_exp_f32_e32 v104, v104
	s_waitcnt lgkmcnt(3)
; #define LAS __attribute__((address_space(3)))
; #define FA_MFMA(a, b, c) __builtin_amdgcn_mfma_f32_32x32x16_bf16((a), (b), (c), 0, 0, 0)
; __device__ __forceinline__ void map_tile(const LAS unsigned char* kp, int ko0, int ko1, const bf16x8 (&qf)[2], const s16x4 (&vlo)[8], const s16x4 (&vhi)[8], f32x16 (&o)[2], float& l) {
;     const bf16x8 k00 = *(const LAS bf16x8*)(kp + ko0), k01 = *(const LAS bf16x8*)(kp + ko1), k10 = *(const LAS bf16x8*)(kp + ko0 + 4096), k11 = *(const LAS bf16x8*)(kp + ko1 + 4096);
;     f32x16 z;
; #pragma unroll
;     for (int i = 0; i < 16; ++i) z[i] = 0.f;
;     f32x16 s0 = FA_MFMA(k00, qf[0], z), s1 = FA_MFMA(k10, qf[0], z);
;     __builtin_amdgcn_sched_group_barrier(0x8, 2, 0);
;     s0 = FA_MFMA(k01, qf[1], s0); s1 = FA_MFMA(k11, qf[1], s1);
; #pragma unroll
;     for (int i = 0; i < 16; ++i) { s0[i] = __builtin_amdgcn_exp2f(s0[i]); s1[i] = __builtin_amdgcn_exp2f(s1[i]); }
;     float a = 0.f, b = 0.f;
; #pragma unroll
;     for (int i = 0; i < 16; ++i) { a += s0[i]; b += s1[i]; }
;     l += a + b;
;     u32x4 pw[4];
; #pragma unroll
;     for (int j = 0; j < 4; ++j) { pw[0][j] = cvtpk(s0[2 * j], s0[2 * j + 1]); pw[1][j] = cvtpk(s0[8 + 2 * j], s0[8 + 2 * j + 1]); pw[2][j] = cvtpk(s1[2 * j], s1[2 * j + 1]); pw[3][j] = cvtpk(s1[8 + 2 * j], s1[8 + 2 * j + 1]); }
; #pragma unroll
;     for (int ks = 0; ks < 4; ++ks)
; #pragma unroll
;         for (int d0 = 0; d0 < 2; ++d0) {
;             const int i = d0 * 4 + ks;
;             const bf16x8 vf = (bf16x8){vlo[i][0], vlo[i][1], vlo[i][2], vlo[i][3], vhi[i][0], vhi[i][1], vhi[i][2], vhi[i][3]};
;             o[d0] = FA_MFMA(__builtin_bit_cast(bf16x8, pw[ks]), vf, o[d0]);
;         }
; }
; template <class Mid> __device__ __forceinline__ void attn_unit(const Mid& mid, LAS unsigned char* lds, const bf16* __restrict__ Qu, const bf16* __restrict__ Kh, const bf16* __restrict__ Vh, int q0, int NT, ...
;     ...
;             const LAS unsigned char* kp = kp0 + sl + sb * SUBB; const LAS unsigned char* vp = vp0 + sl + sb * SUBB;
;             s16x4 vlo[8], vhi[8];
; #pragma unroll
;             for (int i = 0; i < 8; ++i) { vlo[i] = vtr(vp + (i >> 2) * 4096 + (i & 3) * 1024); vhi[i] = vtr(vp + (i >> 2) * 4096 + (i & 3) * 1024 + 512); }
;             map_tile(kp, ko10, ko11, q1f, vlo, vhi, o1, l1);
;             map_tile(kp, ko20, ko21, q2f, vlo, vhi, o2, l2);
	v_mfma_f32_32x32x16_bf16 v[66:81], v[164:167], v[140:143], 0
	ds_read_b128 v[164:167], v192 offset:16384
	v_exp_f32_e32 v105, v105
	v_cvt_pk_bf16_f32 v100, v102, v103
	v_cvt_pk_bf16_f32 v101, v104, v105
	v_exp_f32_e32 v106, v106
	v_exp_f32_e32 v107, v107
	v_mfma_f32_32x32x16_bf16 v[2:17], v[98:101], v[114:117], v[2:17]
	v_exp_f32_e32 v108, v108
	v_exp_f32_e32 v109, v109
	v_cvt_pk_bf16_f32 v102, v106, v107
	v_mfma_f32_32x32x16_bf16 v[18:33], v[98:101], v[184:187], v[18:33]
	v_cvt_pk_bf16_f32 v103, v108, v109
	v_exp_f32_e32 v110, v110
	v_exp_f32_e32 v111, v111
	v_mfma_f32_16x16x32_bf16 v[160:163], v[98:101], v[250:253], v[160:163]
	ds_read_b64_tr_b16 v[114:115], v220 offset:24576
	ds_read_b64_tr_b16 v[116:117], v220 offset:25088
	ds_read_b64_tr_b16 v[184:185], v220 offset:28672
	ds_read_b64_tr_b16 v[186:187], v220 offset:29184
	v_exp_f32_e32 v112, v112
	s_waitcnt lgkmcnt(7)
	v_mfma_f32_32x32x16_bf16 v[66:81], v[168:171], v[136:139], v[66:81]
	ds_read_b128 v[168:171], v193 offset:16384
	v_exp_f32_e32 v113, v113
	v_cvt_pk_bf16_f32 v104, v110, v111
	v_cvt_pk_bf16_f32 v105, v112, v113
	v_exp_f32_e32 v144, v144
	v_exp_f32_e32 v145, v145
	v_mfma_f32_32x32x16_bf16 v[2:17], v[102:105], v[118:121], v[2:17]
	v_exp_f32_e32 v146, v146
	v_exp_f32_e32 v147, v147
	v_cvt_pk_bf16_f32 v144, v144, v145
	v_mfma_f32_32x32x16_bf16 v[18:33], v[102:105], v[188:191], v[18:33]
	v_cvt_pk_bf16_f32 v145, v146, v147
	v_exp_f32_e32 v148, v148
	v_exp_f32_e32 v149, v149
	v_mfma_f32_16x16x32_bf16 v[160:163], v[102:105], v[250:253], v[160:163]
	ds_read_b64_tr_b16 v[118:119], v220 offset:25600
	ds_read_b64_tr_b16 v[120:121], v220 offset:26112
	ds_read_b64_tr_b16 v[188:189], v220 offset:29696
	ds_read_b64_tr_b16 v[190:191], v220 offset:30208
	v_exp_f32_e32 v150, v150
	s_waitcnt lgkmcnt(11)
	v_mfma_f32_32x32x16_bf16 v[82:97], v[172:175], v[140:143], 0
	ds_read_b128 v[172:175], v192 offset:20480
	v_exp_f32_e32 v151, v151
	v_cvt_pk_bf16_f32 v146, v148, v149
	v_cvt_pk_bf16_f32 v147, v150, v151
	v_exp_f32_e32 v152, v152
	v_exp_f32_e32 v153, v153
	v_mfma_f32_32x32x16_bf16 v[2:17], v[144:147], v[122:125], v[2:17]
	v_exp_f32_e32 v154, v154
	v_exp_f32_e32 v155, v155
	v_cvt_pk_bf16_f32 v148, v152, v153
	v_mfma_f32_32x32x16_bf16 v[18:33], v[144:147], v[222:225], v[18:33]
	v_cvt_pk_bf16_f32 v149, v154, v155
	v_exp_f32_e32 v156, v156
	v_exp_f32_e32 v157, v157
	v_mfma_f32_16x16x32_bf16 v[160:163], v[144:147], v[250:253], v[160:163]
	ds_read_b64_tr_b16 v[122:123], v220 offset:26624
	ds_read_b64_tr_b16 v[124:125], v220 offset:27136
	ds_read_b64_tr_b16 v[222:223], v220 offset:30720
	s_waitcnt lgkmcnt(14)
	ds_read_b64_tr_b16 v[224:225], v220 offset:31232
	v_exp_f32_e32 v158, v158
	v_mfma_f32_32x32x16_bf16 v[82:97], v[230:233], v[136:139], v[82:97]
	s_waitcnt lgkmcnt(14)
	ds_read_b128 v[230:233], v193 offset:20480
	v_exp_f32_e32 v159, v159
	v_cvt_pk_bf16_f32 v150, v156, v157
	v_cvt_pk_bf16_f32 v151, v158, v159
	v_exp_f32_e32 v66, v66
	v_exp_f32_e32 v67, v67
	v_mfma_f32_32x32x16_bf16 v[2:17], v[148:151], v[180:183], v[2:17]
	v_exp_f32_e32 v68, v68
	v_exp_f32_e32 v69, v69
	v_cvt_pk_bf16_f32 v66, v66, v67
	v_mfma_f32_32x32x16_bf16 v[18:33], v[148:151], v[226:229], v[18:33]
	v_cvt_pk_bf16_f32 v67, v68, v69
	v_exp_f32_e32 v70, v70
	v_exp_f32_e32 v71, v71
	v_mfma_f32_16x16x32_bf16 v[160:163], v[148:151], v[250:253], v[160:163]
	s_waitcnt lgkmcnt(14)
	ds_read_b64_tr_b16 v[180:181], v220 offset:27648
	s_waitcnt lgkmcnt(14)
	ds_read_b64_tr_b16 v[182:183], v220 offset:28160
	s_waitcnt lgkmcnt(14)
	ds_read_b64_tr_b16 v[226:227], v220 offset:31744
	s_waitcnt lgkmcnt(14)
	ds_read_b64_tr_b16 v[228:229], v220 offset:32256
	v_exp_f32_e32 v72, v72
	v_mfma_f32_32x32x16_bf16 v[98:113], v[164:167], v[132:135], 0
	v_exp_f32_e32 v73, v73
	v_cvt_pk_bf16_f32 v68, v70, v71
	v_cvt_pk_bf16_f32 v69, v72, v73
	v_exp_f32_e32 v74, v74
	v_exp_f32_e32 v75, v75
	v_mfma_f32_32x32x16_bf16 v[50:65], v[66:69], v[114:117], v[50:65]
	v_exp_f32_e32 v76, v76
	v_exp_f32_e32 v77, v77
	v_cvt_pk_bf16_f32 v70, v74, v75
	v_mfma_f32_32x32x16_bf16 v[34:49], v[66:69], v[184:187], v[34:49]
	v_cvt_pk_bf16_f32 v71, v76, v77
	v_exp_f32_e32 v78, v78
	v_exp_f32_e32 v79, v79
	v_mfma_f32_16x16x32_bf16 v[160:163], v[66:69], v[238:241], v[160:163]
	v_exp_f32_e32 v80, v80
	s_waitcnt lgkmcnt(14)
	v_mfma_f32_32x32x16_bf16 v[98:113], v[168:171], v[128:131], v[98:113]
	v_exp_f32_e32 v81, v81
	v_cvt_pk_bf16_f32 v72, v78, v79
	v_cvt_pk_bf16_f32 v73, v80, v81
	v_exp_f32_e32 v82, v82
	v_exp_f32_e32 v83, v83
	s_waitcnt lgkmcnt(12)
	v_mfma_f32_32x32x16_bf16 v[50:65], v[70:73], v[118:121], v[50:65]
	v_exp_f32_e32 v84, v84
	v_exp_f32_e32 v85, v85
	v_cvt_pk_bf16_f32 v82, v82, v83
	s_waitcnt lgkmcnt(10)
	v_mfma_f32_32x32x16_bf16 v[34:49], v[70:73], v[188:191], v[34:49]
	v_cvt_pk_bf16_f32 v83, v84, v85
	v_exp_f32_e32 v86, v86
	v_exp_f32_e32 v87, v87
	v_mfma_f32_16x16x32_bf16 v[160:163], v[70:73], v[238:241], v[160:163]
	v_exp_f32_e32 v88, v88
	s_waitcnt lgkmcnt(9)
	v_mfma_f32_32x32x16_bf16 v[144:159], v[172:175], v[132:135], 0
	v_exp_f32_e32 v89, v89
	v_cvt_pk_bf16_f32 v84, v86, v87
	v_cvt_pk_bf16_f32 v85, v88, v89
	v_exp_f32_e32 v90, v90
	v_exp_f32_e32 v91, v91
	s_waitcnt lgkmcnt(7)
	v_mfma_f32_32x32x16_bf16 v[50:65], v[82:85], v[122:125], v[50:65]
	v_exp_f32_e32 v92, v92
	v_exp_f32_e32 v93, v93
	v_cvt_pk_bf16_f32 v86, v90, v91
	s_waitcnt lgkmcnt(5)
	v_mfma_f32_32x32x16_bf16 v[34:49], v[82:85], v[222:225], v[34:49]
	v_cvt_pk_bf16_f32 v87, v92, v93
	v_exp_f32_e32 v94, v94
	v_exp_f32_e32 v95, v95
	v_mfma_f32_16x16x32_bf16 v[160:163], v[82:85], v[238:241], v[160:163]
	v_exp_f32_e32 v96, v96
	s_waitcnt lgkmcnt(4)
; #define LAS __attribute__((address_space(3)))
; #define FA_MFMA(a, b, c) __builtin_amdgcn_mfma_f32_32x32x16_bf16((a), (b), (c), 0, 0, 0)
; __device__ __forceinline__ void map_tile(const LAS unsigned char* kp, int ko0, int ko1, const bf16x8 (&qf)[2], const s16x4 (&vlo)[8], const s16x4 (&vhi)[8], f32x16 (&o)[2], float& l) {
;     const bf16x8 k00 = *(const LAS bf16x8*)(kp + ko0), k01 = *(const LAS bf16x8*)(kp + ko1), k10 = *(const LAS bf16x8*)(kp + ko0 + 4096), k11 = *(const LAS bf16x8*)(kp + ko1 + 4096);
;     f32x16 z;
; #pragma unroll
;     for (int i = 0; i < 16; ++i) z[i] = 0.f;
;     f32x16 s0 = FA_MFMA(k00, qf[0], z), s1 = FA_MFMA(k10, qf[0], z);
;     __builtin_amdgcn_sched_group_barrier(0x8, 2, 0);
;     s0 = FA_MFMA(k01, qf[1], s0); s1 = FA_MFMA(k11, qf[1], s1);
; #pragma unroll
;     for (int i = 0; i < 16; ++i) { s0[i] = __builtin_amdgcn_exp2f(s0[i]); s1[i] = __builtin_amdgcn_exp2f(s1[i]); }
;     float a = 0.f, b = 0.f;
; #pragma unroll
;     for (int i = 0; i < 16; ++i) { a += s0[i]; b += s1[i]; }
;     l += a + b;
;     u32x4 pw[4];
; #pragma unroll
;     for (int j = 0; j < 4; ++j) { pw[0][j] = cvtpk(s0[2 * j], s0[2 * j + 1]); pw[1][j] = cvtpk(s0[8 + 2 * j], s0[8 + 2 * j + 1]); pw[2][j] = cvtpk(s1[2 * j], s1[2 * j + 1]); pw[3][j] = cvtpk(s1[8 + 2 * j], s1[8 + 2 * j + 1]); }
; #pragma unroll
;     for (int ks = 0; ks < 4; ++ks)
; #pragma unroll
;         for (int d0 = 0; d0 < 2; ++d0) {
;             const int i = d0 * 4 + ks;
;             const bf16x8 vf = (bf16x8){vlo[i][0], vlo[i][1], vlo[i][2], vlo[i][3], vhi[i][0], vhi[i][1], vhi[i][2], vhi[i][3]};
;             o[d0] = FA_MFMA(__builtin_bit_cast(bf16x8, pw[ks]), vf, o[d0]);
;         }
; }
; template <class Mid> __device__ __forceinline__ void attn_unit(const Mid& mid, LAS unsigned char* lds, const bf16* __restrict__ Qu, const bf16* __restrict__ Kh, const bf16* __restrict__ Vh, int q0, int NT, ...
;     ...
;     asm volatile("s_waitcnt vmcnt(0) lgkmcnt(0)\n\ts_barrier" ::: "memory");
;     f32x4 xv[32]; mid.load(xv);
;     l1 += __shfl_xor(l1, 32); l2 += __shfl_xor(l2, 32);
;     int lane_e = lane; asm volatile("" : "+v"(lane_e));
;     const int r32e = lane_e & 31, hie = lane_e >> 5;
;     LAS float* wsf = (LAS float*)(lds + FA_WS) + wid * 64;
;     if (hie == 0) { wsf[r32e] = 1.0f / l1; wsf[32 + r32e] = lam / l2; }
	v_mfma_f32_32x32x16_bf16 v[144:159], v[230:233], v[128:131], v[144:159]
	v_exp_f32_e32 v97, v97
	v_cvt_pk_bf16_f32 v88, v94, v95
	v_cvt_pk_bf16_f32 v89, v96, v97
	v_exp_f32_e32 v98, v98
	v_exp_f32_e32 v99, v99
	s_waitcnt lgkmcnt(2)
	v_mfma_f32_32x32x16_bf16 v[50:65], v[86:89], v[180:183], v[50:65]
	v_exp_f32_e32 v100, v100
	v_exp_f32_e32 v101, v101
	v_cvt_pk_bf16_f32 v98, v98, v99
	s_waitcnt lgkmcnt(0)
	v_mfma_f32_32x32x16_bf16 v[34:49], v[86:89], v[226:229], v[34:49]
	v_cvt_pk_bf16_f32 v99, v100, v101
	v_exp_f32_e32 v102, v102
	v_exp_f32_e32 v103, v103
	v_mfma_f32_16x16x32_bf16 v[160:163], v[86:89], v[238:241], v[160:163]
	v_exp_f32_e32 v104, v104
	v_exp_f32_e32 v105, v105
	v_cvt_pk_bf16_f32 v100, v102, v103
	v_cvt_pk_bf16_f32 v101, v104, v105
	v_exp_f32_e32 v106, v106
	v_exp_f32_e32 v107, v107
	v_mfma_f32_32x32x16_bf16 v[2:17], v[98:101], v[114:117], v[2:17]
	v_exp_f32_e32 v108, v108
	v_exp_f32_e32 v109, v109
	v_cvt_pk_bf16_f32 v102, v106, v107
	v_mfma_f32_32x32x16_bf16 v[18:33], v[98:101], v[184:187], v[18:33]
	v_cvt_pk_bf16_f32 v103, v108, v109
	v_exp_f32_e32 v110, v110
	v_exp_f32_e32 v111, v111
	v_mfma_f32_16x16x32_bf16 v[160:163], v[98:101], v[250:253], v[160:163]
	v_exp_f32_e32 v112, v112
	v_exp_f32_e32 v113, v113
	v_cvt_pk_bf16_f32 v104, v110, v111
	v_cvt_pk_bf16_f32 v105, v112, v113
	v_exp_f32_e32 v144, v144
	v_exp_f32_e32 v145, v145
	v_mfma_f32_32x32x16_bf16 v[2:17], v[102:105], v[118:121], v[2:17]
	v_exp_f32_e32 v146, v146
	v_exp_f32_e32 v147, v147
	v_cvt_pk_bf16_f32 v144, v144, v145
	v_mfma_f32_32x32x16_bf16 v[18:33], v[102:105], v[188:191], v[18:33]
	v_cvt_pk_bf16_f32 v145, v146, v147
	v_exp_f32_e32 v148, v148
	v_exp_f32_e32 v149, v149
	v_mfma_f32_16x16x32_bf16 v[160:163], v[102:105], v[250:253], v[160:163]
	v_exp_f32_e32 v150, v150
	v_exp_f32_e32 v151, v151
	v_cvt_pk_bf16_f32 v146, v148, v149
	v_cvt_pk_bf16_f32 v147, v150, v151
	v_exp_f32_e32 v152, v152
	v_exp_f32_e32 v153, v153
	v_mfma_f32_32x32x16_bf16 v[2:17], v[144:147], v[122:125], v[2:17]
	v_exp_f32_e32 v154, v154
	v_exp_f32_e32 v155, v155
	v_cvt_pk_bf16_f32 v148, v152, v153
	v_mfma_f32_32x32x16_bf16 v[18:33], v[144:147], v[222:225], v[18:33]
	v_cvt_pk_bf16_f32 v149, v154, v155
	v_exp_f32_e32 v156, v156
	v_exp_f32_e32 v157, v157
	v_mfma_f32_16x16x32_bf16 v[160:163], v[144:147], v[250:253], v[160:163]
	v_exp_f32_e32 v158, v158
	v_exp_f32_e32 v159, v159
	v_cvt_pk_bf16_f32 v150, v156, v157
	v_cvt_pk_bf16_f32 v151, v158, v159
	s_nop 1
	v_mfma_f32_32x32x16_bf16 v[2:17], v[148:151], v[180:183], v[2:17]
	v_mfma_f32_32x32x16_bf16 v[18:33], v[148:151], v[226:229], v[18:33]
	v_mfma_f32_16x16x32_bf16 v[160:163], v[148:151], v[250:253], v[160:163]
	s_add_i32 s12, s70, 0x8000
	s_cmp_lt_i32 s70, 0x10000
	s_cselect_b32 s70, s12, 0
	s_add_i32 s71, s71, 1
	s_cmp_eq_u32 s71, 34
	s_cbranch_scc0 .LBB0_1357
	s_nop 15
	v_readfirstlane_b32 s100, v0
	v_mbcnt_lo_u32_b32 v198, -1, 0
	v_mbcnt_hi_u32_b32 v198, -1, v198
	s_and_b32 s100, s100, 0x1c0
	s_lshl_b32 s100, s100, 2
	s_add_i32 s100, s100, 0x20000
	v_and_b32_e32 v199, 15, v198
	v_lshrrev_b32_e32 v202, 4, v198
	v_lshlrev_b32_e32 v203, 6, v199
	v_lshl_add_u32 v203, v202, 4, v203
	v_add_u32_e32 v203, s100, v203
	v_and_b32_e32 v199, 31, v198
	v_lshl_add_u32 v202, v199, 2, s100
	s_mov_b64 s[98:99], exec
	s_mov_b32 exec_lo, 0xf000f
	s_mov_b32 exec_hi, 0xf000f
	ds_write_b128 v203, v[160:163]
	s_mov_b64 exec, s[98:99]
	s_waitcnt lgkmcnt(0)
	ds_read_b32 v201, v202
	ds_read_b32 v200, v202 offset:128
	s_waitcnt lgkmcnt(0)
	v_mul_f32_e32 v200, 0.5, v200
	v_mul_f32_e32 v201, 0.5, v201
	s_lshl_b32 s24, s67, 6
	s_lshl_b32 s12, s48, 5
	s_and_b32 s67, s24, 0x3c0
	s_cmpk_lt_i32 s48, 0x3000
	s_cselect_b64 s[24:25], -1, 0
	s_and_b32 s12, s12, 32
	s_waitcnt vmcnt(0) lgkmcnt(0)
	s_barrier
	s_or_b32 s12, s67, s12
	s_cmpk_gt_i32 s48, 0x2fff
	v_or_b32_e32 v198, s62, v209
	s_cbranch_scc1 .LBB0_1362
	s_mul_i32 s67, s28, s12
	s_lshl_b32 s67, s67, 2
	s_add_u32 s68, s26, s67
	s_addc_u32 s69, s27, 0
	s_or_b32 s67, s12, 1
	v_mov_b32_e32 v199, v197
	s_mul_i32 s67, s28, s67
	v_lshlrev_b64 v[186:187], 2, v[198:199]
	s_lshl_b32 s67, s67, 2
	v_lshl_add_u64 v[66:67], s[68:69], 0, v[186:187]
	s_add_u32 s68, s26, s67
	s_addc_u32 s69, s27, 0
	s_or_b32 s67, s12, 2
	s_mul_i32 s67, s28, s67
	s_lshl_b32 s67, s67, 2
	v_lshl_add_u64 v[68:69], s[68:69], 0, v[186:187]
	s_add_u32 s68, s26, s67
	s_addc_u32 s69, s27, 0
	s_or_b32 s67, s12, 3
	s_mul_i32 s67, s28, s67
	s_lshl_b32 s67, s67, 2
	v_lshl_add_u64 v[74:75], s[68:69], 0, v[186:187]
	s_add_u32 s68, s26, s67
	s_addc_u32 s69, s27, 0
	s_or_b32 s67, s12, 4
	s_mul_i32 s67, s28, s67
	s_lshl_b32 s67, s67, 2
	v_lshl_add_u64 v[76:77], s[68:69], 0, v[186:187]
	s_add_u32 s68, s26, s67
	s_addc_u32 s69, s27, 0
	s_or_b32 s67, s12, 5
	s_mul_i32 s67, s28, s67
	s_lshl_b32 s67, s67, 2
	v_lshl_add_u64 v[82:83], s[68:69], 0, v[186:187]
	s_add_u32 s68, s26, s67
	s_addc_u32 s69, s27, 0
	s_or_b32 s67, s12, 6
	s_mul_i32 s67, s28, s67
	s_lshl_b32 s67, s67, 2
	v_lshl_add_u64 v[84:85], s[68:69], 0, v[186:187]
	s_add_u32 s68, s26, s67
	s_addc_u32 s69, s27, 0
	s_or_b32 s67, s12, 7
	s_mul_i32 s67, s28, s67
	s_lshl_b32 s67, s67, 2
	v_lshl_add_u64 v[90:91], s[68:69], 0, v[186:187]
	s_add_u32 s68, s26, s67
	s_addc_u32 s69, s27, 0
	s_or_b32 s67, s12, 8
	s_mul_i32 s67, s28, s67
	s_lshl_b32 s67, s67, 2
	v_lshl_add_u64 v[92:93], s[68:69], 0, v[186:187]
	s_add_u32 s68, s26, s67
	s_addc_u32 s69, s27, 0
	s_or_b32 s67, s12, 9
	s_mul_i32 s67, s28, s67
	s_lshl_b32 s67, s67, 2
	v_lshl_add_u64 v[98:99], s[68:69], 0, v[186:187]
	s_add_u32 s68, s26, s67
	s_addc_u32 s69, s27, 0
	s_or_b32 s67, s12, 10
	s_mul_i32 s67, s28, s67
	s_lshl_b32 s67, s67, 2
;     __device__ __forceinline__ void load(f32x4 (&v)[32]) const { if (on) {
; #pragma unroll
;         for (int i = 0; i < 32; ++i) v[i] = *(const f32x4*)(src + (size_t)(k0 + i) * N + n0); } }
	v_lshl_add_u64 v[100:101], s[68:69], 0, v[186:187]
	s_add_u32 s68, s26, s67
	s_addc_u32 s69, s27, 0
	s_or_b32 s67, s12, 11
	s_mul_i32 s67, s28, s67
	s_lshl_b32 s67, s67, 2
	v_lshl_add_u64 v[106:107], s[68:69], 0, v[186:187]
	s_add_u32 s68, s26, s67
	s_addc_u32 s69, s27, 0
	s_or_b32 s67, s12, 12
	s_mul_i32 s67, s28, s67
	s_lshl_b32 s67, s67, 2
	v_lshl_add_u64 v[108:109], s[68:69], 0, v[186:187]
	s_add_u32 s68, s26, s67
	s_addc_u32 s69, s27, 0
	s_or_b32 s67, s12, 13
	s_mul_i32 s67, s28, s67
	s_lshl_b32 s67, s67, 2
	v_lshl_add_u64 v[114:115], s[68:69], 0, v[186:187]
	s_add_u32 s68, s26, s67
	s_addc_u32 s69, s27, 0
	s_or_b32 s67, s12, 14
	s_mul_i32 s67, s28, s67
	s_lshl_b32 s67, s67, 2
	v_lshl_add_u64 v[116:117], s[68:69], 0, v[186:187]
	s_add_u32 s68, s26, s67
	s_addc_u32 s69, s27, 0
	s_or_b32 s67, s12, 15
	s_mul_i32 s67, s28, s67
	s_lshl_b32 s67, s67, 2
	v_lshl_add_u64 v[122:123], s[68:69], 0, v[186:187]
	s_add_u32 s68, s26, s67
	s_addc_u32 s69, s27, 0
	s_or_b32 s67, s12, 16
	s_mul_i32 s67, s28, s67
	s_lshl_b32 s67, s67, 2
	v_lshl_add_u64 v[124:125], s[68:69], 0, v[186:187]
	s_add_u32 s68, s26, s67
	s_addc_u32 s69, s27, 0
	s_or_b32 s67, s12, 17
	s_mul_i32 s67, s28, s67
	s_lshl_b32 s67, s67, 2
	v_lshl_add_u64 v[126:127], s[68:69], 0, v[186:187]
	s_add_u32 s68, s26, s67
	s_addc_u32 s69, s27, 0
	s_or_b32 s67, s12, 18
	s_mul_i32 s67, s28, s67
	s_lshl_b32 s67, s67, 2
	v_lshl_add_u64 v[128:129], s[68:69], 0, v[186:187]
	s_add_u32 s68, s26, s67
	s_addc_u32 s69, s27, 0
	s_or_b32 s67, s12, 19
	s_mul_i32 s67, s28, s67
	s_lshl_b32 s67, s67, 2
	v_lshl_add_u64 v[138:139], s[68:69], 0, v[186:187]
	s_add_u32 s68, s26, s67
	s_addc_u32 s69, s27, 0
	s_or_b32 s67, s12, 20
	s_mul_i32 s67, s28, s67
	s_lshl_b32 s67, s67, 2
	v_lshl_add_u64 v[140:141], s[68:69], 0, v[186:187]
	s_add_u32 s68, s26, s67
	s_addc_u32 s69, s27, 0
	s_or_b32 s67, s12, 21
	s_mul_i32 s67, s28, s67
	s_lshl_b32 s67, s67, 2
	v_lshl_add_u64 v[146:147], s[68:69], 0, v[186:187]
	s_add_u32 s68, s26, s67
	s_addc_u32 s69, s27, 0
	s_or_b32 s67, s12, 22
	s_mul_i32 s67, s28, s67
	s_lshl_b32 s67, s67, 2
	v_lshl_add_u64 v[148:149], s[68:69], 0, v[186:187]
	s_add_u32 s68, s26, s67
	s_addc_u32 s69, s27, 0
	s_or_b32 s67, s12, 23
	s_mul_i32 s67, s28, s67
	s_lshl_b32 s67, s67, 2
	v_lshl_add_u64 v[154:155], s[68:69], 0, v[186:187]
	s_add_u32 s68, s26, s67
	s_addc_u32 s69, s27, 0
	s_or_b32 s67, s12, 24
	s_mul_i32 s67, s28, s67
	s_lshl_b32 s67, s67, 2
	v_lshl_add_u64 v[156:157], s[68:69], 0, v[186:187]
	s_add_u32 s68, s26, s67
	s_addc_u32 s69, s27, 0
	s_or_b32 s67, s12, 25
	s_mul_i32 s67, s28, s67
	s_lshl_b32 s67, s67, 2
	v_lshl_add_u64 v[162:163], s[68:69], 0, v[186:187]
	s_add_u32 s68, s26, s67
	s_addc_u32 s69, s27, 0
	s_or_b32 s67, s12, 26
	s_mul_i32 s67, s28, s67
	s_lshl_b32 s67, s67, 2
	v_lshl_add_u64 v[164:165], s[68:69], 0, v[186:187]
	s_add_u32 s68, s26, s67
	s_addc_u32 s69, s27, 0
	s_or_b32 s67, s12, 27
	s_mul_i32 s67, s28, s67
	s_lshl_b32 s67, s67, 2
	v_lshl_add_u64 v[170:171], s[68:69], 0, v[186:187]
	s_add_u32 s68, s26, s67
	s_addc_u32 s69, s27, 0
	s_or_b32 s67, s12, 28
	s_mul_i32 s67, s28, s67
	s_lshl_b32 s67, s67, 2
	v_lshl_add_u64 v[172:173], s[68:69], 0, v[186:187]
	s_add_u32 s68, s26, s67
	s_addc_u32 s69, s27, 0
	s_or_b32 s67, s12, 29
	s_mul_i32 s67, s28, s67
	s_lshl_b32 s67, s67, 2
	v_lshl_add_u64 v[178:179], s[68:69], 0, v[186:187]
	s_add_u32 s68, s26, s67
	s_addc_u32 s69, s27, 0
	s_or_b32 s67, s12, 30
	s_mul_i32 s67, s28, s67
	s_lshl_b32 s67, s67, 2
	v_lshl_add_u64 v[180:181], s[68:69], 0, v[186:187]
	s_add_u32 s68, s26, s67
	s_addc_u32 s69, s27, 0
	s_or_b32 s67, s12, 31
	s_mul_i32 s28, s28, s67
	s_lshl_b32 s28, s28, 2
	s_add_u32 s26, s26, s28
	s_addc_u32 s27, s27, 0
	v_lshl_add_u64 v[188:189], s[68:69], 0, v[186:187]
	v_lshl_add_u64 v[186:187], s[26:27], 0, v[186:187]
	global_load_dwordx4 v[70:73], v[66:67], off
	s_nop 0
	global_load_dwordx4 v[66:69], v[68:69], off
	s_nop 0
	global_load_dwordx4 v[78:81], v[74:75], off
	s_nop 0
	global_load_dwordx4 v[74:77], v[76:77], off
	s_nop 0
	global_load_dwordx4 v[86:89], v[82:83], off
	s_nop 0
	global_load_dwordx4 v[82:85], v[84:85], off
	s_nop 0
	global_load_dwordx4 v[94:97], v[90:91], off
	s_nop 0
	global_load_dwordx4 v[90:93], v[92:93], off
	s_nop 0
	global_load_dwordx4 v[102:105], v[98:99], off
	s_nop 0
	global_load_dwordx4 v[98:101], v[100:101], off
	s_nop 0
	global_load_dwordx4 v[110:113], v[106:107], off
	s_nop 0
	global_load_dwordx4 v[106:109], v[108:109], off
	s_nop 0
	global_load_dwordx4 v[118:121], v[114:115], off
	s_nop 0
	global_load_dwordx4 v[114:117], v[116:117], off
	s_nop 0
	global_load_dwordx4 v[130:133], v[122:123], off
	s_nop 0
	global_load_dwordx4 v[122:125], v[124:125], off
	s_nop 0
	global_load_dwordx4 v[134:137], v[126:127], off
	s_nop 0
	global_load_dwordx4 v[126:129], v[128:129], off
	s_nop 0
	global_load_dwordx4 v[142:145], v[138:139], off
	s_nop 0
	global_load_dwordx4 v[138:141], v[140:141], off
	s_nop 0
	global_load_dwordx4 v[150:153], v[146:147], off
	s_nop 0
	global_load_dwordx4 v[146:149], v[148:149], off
	s_nop 0
	global_load_dwordx4 v[158:161], v[154:155], off
	s_nop 0
	global_load_dwordx4 v[154:157], v[156:157], off
	s_nop 0
	global_load_dwordx4 v[166:169], v[162:163], off
	s_nop 0
	global_load_dwordx4 v[162:165], v[164:165], off
	s_nop 0
	global_load_dwordx4 v[174:177], v[170:171], off
	s_nop 0
	global_load_dwordx4 v[170:173], v[172:173], off
	s_nop 0
	global_load_dwordx4 v[182:185], v[178:179], off
	s_nop 0
	global_load_dwordx4 v[178:181], v[180:181], off
	s_nop 0
	global_load_dwordx4 v[190:193], v[188:189], off
	s_nop 0
	global_load_dwordx4 v[186:189], v[186:187], off
